# sp3 (SSD chunk outputs): tile order permuted so that the 8 (head, half) tiles of a chunk run on one XCD
# speedup vs baseline: 1.0502x; 1.0047x over previous
; __device__ __forceinline__ void ssd_s3(const Ctx& c, int layer, int tile, unsigned char* lds) {
;     const int half = tile & 1, h = (tile >> 1) & 3, j = (tile >> 3) % NCH, b = tile / (8 * NCH);
; __global__ void __launch_bounds__(NTHR, 2) mk_fwd(Params prm) {
;     ...
;             case 3: for (int t = bid; t < 1088 + 320; t += G) { asm volatile("" : "+v"(c.tid)); asm volatile("" : "+s"(c.p)); if (t < 1088) ssd_s3(c, layer, t, smem_raw); else s5_gemm_y(c, layer, t - 1088, smem_raw); } break;
.LBB0_322:
	v_readlane_b32 s58, v254, 5
	s_nop 0
	v_readlane_b32 s6, v251, 3
	s_add_i32 s58, s58, s3
	s_add_i32 s57, s57, s3
	s_add_i32 s56, s56, s6
	s_cmpk_gt_i32 s58, 0x57f
	s_cbranch_scc1 .LBB0_344
.LBB0_323:
	v_writelane_b32 v254, s58, 5
	s_cmpk_gt_i32 s58, 0x43f
	s_cbranch_scc1 .Ls3_noperm
	s_and_b32 s6, s58, 7
	s_lshr_b32 s7, s58, 3
	s_mulk_i32 s6, 0x88
	s_add_i32 s58, s6, s7
